# P3 conversion fill loop: the loop-head wait leaves the previous tile's stores outstanding
# speedup vs baseline: 1.0047x; 1.0012x over previous
; __device__ __forceinline__ void conv8_fill(const Ctx& X, int base, int rank, int nblk, int n) { conv8b_run(X, (base >> 3) + rank, nblk, n); }
; #define SEAM(k) do { if (IN(k) && IN((k) + 1)) xcd_barrier(bar); } while (0)
; __device__ __forceinline__ Cvb conv8b_dec(const Ctx& X, int bit) { Cvb c; int kb, nb;
;     if (bit < I_GU8 / 8) { const int e = bit >> 8, r = bit & 255; kb = r >> 4; nb = r & 15; c.N = 2 * DFF; c.W = XP_w_gu(X) + (size_t)e * D * (2 * DFF); c.WT = XP_WguT(X) + (size_t)e * 16 * PAN_GU + (size_t)kb * PAN_GU; }
;     else { const int b2 = bit - I_GU8 / 8, e = b2 >> 7, r = b2 & 127; kb = r >> 3; nb = r & 7; c.N = D; c.W = XP_w_d(X) + (size_t)e * DFF * D; c.WT = XP_WdT(X) + (size_t)e * 16 * PAN_D + (size_t)kb * PAN_D; }
;     c.W += (size_t)(kb * 128 + 16 * X.wave) * c.N + nb * 256 + 4 * X.lane;
;     c.WT += (size_t)(nb * 256 + 32 * X.wave + (X.lane >> 3)) * 128 + 16 * (X.lane & 7);
;     return c; }
; __device__ __forceinline__ void conv8b_run(const Ctx& X, int first, int step, int count) {
;     if (count <= 0) return;
;     f32x4 v[16];
;     Cvb c = conv8b_dec(X, first), cn = c;
; #pragma unroll
;     for (int i = 0; i < 16; ++i) v[i] = __builtin_nontemporal_load((const f32x4*)(c.W + (size_t)i * c.N));
; __global__ void __launch_bounds__(NTHR, 2) fwd(Args args) {
;     ...
;     if (IN(3)) { p3_scan(X); if (X.G == 256 && X.bid >= 192) conv8_fill(X, FILL_B3, X.bid - 192, FILL_W3 / NWAVES, FILL_N3); } SEAM(3);
.LBB0_474:
	s_or_b64 exec, exec, s[6:7]
	s_cmpk_lg_i32 s92, 0x100
	s_cselect_b64 s[2:3], -1, 0
	s_cmpk_lt_i32 s87, 0xc0
	s_cselect_b64 s[6:7], -1, 0
	s_or_b64 s[2:3], s[6:7], s[2:3]
	s_and_b64 vcc, exec, s[2:3]
	s_cbranch_vccnz .LBB0_480
	s_load_dwordx2 s[6:7], s[0:1], 0x80
	s_add_i32 s2, s87, 0x900
	s_lshr_b32 s2, s2, 7
	s_mov_b32 s3, 0
	s_bfe_u32 s13, s87, 0x40003
	s_lshl_b64 s[8:9], s[2:3], 24
	s_waitcnt lgkmcnt(0)
	s_add_u32 s14, s6, s8
	s_addc_u32 s15, s7, s9
	s_add_u32 s10, s90, 0x50000000
	s_addc_u32 s11, s91, 0
	s_lshl_b64 s[6:7], s[2:3], 22
	s_add_u32 s2, s10, s6
	s_addc_u32 s7, s11, s7
	s_lshl_b32 s6, s13, 18
	s_add_u32 s6, s2, s6
	s_addc_u32 s7, s7, 0
	s_lshl_b32 s2, s87, 8
	s_lshl_b32 s16, s93, 5
	s_and_b32 s17, s2, 0x700
	s_add_i32 s2, s16, s17
	v_lshrrev_b32_e32 v75, 3, v194
	v_or_b32_e32 v66, s2, v75
	s_lshl_b32 s12, s93, 4
	s_lshl_b32 s2, s13, 7
	s_add_i32 s2, s12, s2
	s_lshl_b64 s[8:9], s[2:3], 13
	s_add_u32 s2, s14, s8
	s_addc_u32 s9, s15, s9
	s_lshl_b32 s8, s17, 2
	v_mov_b32_e32 v67, 0
	s_add_u32 s8, s2, s8
	v_lshlrev_b64 v[68:69], 7, v[66:67]
	s_addc_u32 s9, s9, 0
	v_lshlrev_b32_e32 v66, 4, v194
	s_waitcnt vmcnt(3)
	v_lshl_add_u64 v[30:31], s[8:9], 0, v[66:67]
	s_mov_b32 s2, 0x1e000
	v_add_co_u32_e32 v6, vcc, s2, v30
	s_mov_b32 s2, 0x1c000
	s_nop 0
	v_addc_co_u32_e32 v7, vcc, 0, v31, vcc
	v_add_co_u32_e32 v8, vcc, s2, v30
	s_mov_b32 s2, 0x1a000
	s_nop 0
	v_addc_co_u32_e32 v9, vcc, 0, v31, vcc
	v_add_co_u32_e32 v10, vcc, s2, v30
	s_mov_b32 s2, 0x18000
	s_nop 0
	v_addc_co_u32_e32 v11, vcc, 0, v31, vcc
	v_add_co_u32_e32 v12, vcc, s2, v30
	s_mov_b32 s2, 0x16000
	s_nop 0
	v_addc_co_u32_e32 v13, vcc, 0, v31, vcc
	v_add_co_u32_e32 v14, vcc, s2, v30
	s_mov_b32 s2, 0x14000
	s_nop 0
	v_addc_co_u32_e32 v15, vcc, 0, v31, vcc
	v_add_co_u32_e32 v16, vcc, s2, v30
	s_mov_b32 s2, 0x12000
	s_nop 0
	v_addc_co_u32_e32 v17, vcc, 0, v31, vcc
	v_add_co_u32_e32 v18, vcc, s2, v30
	s_mov_b32 s2, 0x10000
	s_nop 0
	v_addc_co_u32_e32 v19, vcc, 0, v31, vcc
	v_add_co_u32_e32 v20, vcc, s2, v30
	s_mov_b32 s2, 0xe000
	s_nop 0
	v_addc_co_u32_e32 v21, vcc, 0, v31, vcc
	v_add_co_u32_e32 v22, vcc, s2, v30
	s_mov_b32 s2, 0xc000
	s_nop 0
	v_addc_co_u32_e32 v23, vcc, 0, v31, vcc
	v_add_co_u32_e32 v24, vcc, s2, v30
	s_mov_b32 s2, 0xa000
	s_nop 0
	v_addc_co_u32_e32 v25, vcc, 0, v31, vcc
	v_add_co_u32_e32 v26, vcc, s2, v30
	s_mov_b32 s2, 0x8000
	s_nop 0
	v_addc_co_u32_e32 v27, vcc, 0, v31, vcc
	v_add_co_u32_e32 v28, vcc, s2, v30
	s_movk_i32 s2, 0x6000
	s_nop 0
	v_addc_co_u32_e32 v29, vcc, 0, v31, vcc
	v_add_co_u32_e32 v32, vcc, s2, v30
	s_movk_i32 s2, 0x4000
	s_nop 0
	v_addc_co_u32_e32 v33, vcc, 0, v31, vcc
	s_waitcnt vmcnt(0)
	v_add_co_u32_e32 v62, vcc, s2, v30
	s_movk_i32 s2, 0x2000
	s_nop 0
	v_addc_co_u32_e32 v63, vcc, 0, v31, vcc
	v_add_co_u32_e32 v70, vcc, s2, v30
	global_load_dwordx4 v[34:37], v[6:7], off nt
	global_load_dwordx4 v[2:5], v[8:9], off nt
	v_addc_co_u32_e32 v71, vcc, 0, v31, vcc
	global_load_dwordx4 v[38:41], v[10:11], off nt
	global_load_dwordx4 v[6:9], v[12:13], off nt
	global_load_dwordx4 v[42:45], v[14:15], off nt
	s_nop 0
	global_load_dwordx4 v[10:13], v[16:17], off nt
	global_load_dwordx4 v[46:49], v[18:19], off nt
	s_nop 0
	global_load_dwordx4 v[14:17], v[20:21], off nt
	global_load_dwordx4 v[50:53], v[22:23], off nt
	s_nop 0
	global_load_dwordx4 v[18:21], v[24:25], off nt
	global_load_dwordx4 v[54:57], v[26:27], off nt
	s_nop 0
	global_load_dwordx4 v[22:25], v[28:29], off nt
	global_load_dwordx4 v[58:61], v[32:33], off nt
	s_nop 0
	global_load_dwordx4 v[26:29], v[62:63], off nt
	global_load_dwordx4 v[30:33], v[70:71], off nt
	s_nop 0
	global_load_dwordx4 v[62:65], v66, s[8:9] nt
	v_lshlrev_b32_e32 v66, 4, v0
	v_lshl_add_u64 v[70:71], s[6:7], 0, v[68:69]
	v_and_b32_e32 v68, 0x70, v66
	v_mov_b32_e32 v69, v67
	v_or_b32_e32 v66, s16, v75
	s_movk_i32 s2, 0x90
	v_lshl_add_u64 v[72:73], v[70:71], 0, v[68:69]
	v_lshlrev_b32_e32 v74, 2, v194
	v_mul_lo_u32 v77, v66, s2
	v_add_u32_e32 v66, s17, v66
	v_mul_u32_u24_e32 v76, 0x240, v194
	v_lshlrev_b64 v[70:71], 7, v[66:67]
	s_add_i32 s13, s87, 0x2940
	s_mov_b32 s14, 0xc3e00000
	s_lshl_b32 s15, s17, 2
	v_lshlrev_b32_e32 v66, 2, v74
	v_mov_b32_e32 v78, 0x43e00000
	s_mov_b32 s16, 0
	v_mov_b64_e32 v[74:75], v[72:73]
	s_waitcnt vmcnt(0)
	s_branch .LBB0_477

; #define LAS __attribute__((address_space(3)))
; __device__ __forceinline__ void conv8b_run(const Ctx& X, int first, int step, int count) {
;     ...
;         LAS uchar* buf = X.lds + (j & 1) * CVT_BUF;
; #pragma unroll
;         for (int q = 0; q < 4; ++q) { u32x4 o;
;             o.x = pk_fp8x4(v[0][q] * W8_SCALE, v[1][q] * W8_SCALE, v[2][q] * W8_SCALE, v[3][q] * W8_SCALE); o.y = pk_fp8x4(v[4][q] * W8_SCALE, v[5][q] * W8_SCALE, v[6][q] * W8_SCALE, v[7][q] * W8_SCALE);
;             o.z = pk_fp8x4(v[8][q] * W8_SCALE, v[9][q] * W8_SCALE, v[10][q] * W8_SCALE, v[11][q] * W8_SCALE); o.w = pk_fp8x4(v[12][q] * W8_SCALE, v[13][q] * W8_SCALE, v[14][q] * W8_SCALE, v[15][q] * W8_SCALE);
;             *(LAS u32x4*)(buf + (4 * X.lane + q) * CVT_STRIDE + 16 * X.wave) = o; }
;         if (j + 1 < count) { cn = conv8b_dec(X, first + (j + 1) * step);
.LBB0_477:
	s_waitcnt vmcnt(4)
	v_mul_f32_e32 v79, 0x42800000, v62
	v_mul_f32_e32 v80, 0x42800000, v30
	v_med3_f32 v79, v79, s14, v78
	v_med3_f32 v82, v80, s14, v78
	v_mov_b32_e32 v80, 0
	v_cvt_pk_fp8_f32 v80, v79, v82
	v_mul_f32_e32 v81, 0x42800000, v26
	v_mul_f32_e32 v79, 0x42800000, v58
	v_med3_f32 v81, v81, s14, v78
	v_med3_f32 v79, v79, s14, v78
	v_cvt_pk_fp8_f32 v80, v81, v79 op_sel:[0,0,1]
	v_mul_f32_e32 v79, 0x42800000, v22
	v_mul_f32_e32 v81, 0x42800000, v54
	v_med3_f32 v79, v79, s14, v78
	v_med3_f32 v83, v81, s14, v78
	v_mov_b32_e32 v81, 0
	v_cvt_pk_fp8_f32 v81, v79, v83
	v_mul_f32_e32 v82, 0x42800000, v18
	v_mul_f32_e32 v79, 0x42800000, v50
	v_med3_f32 v82, v82, s14, v78
	v_med3_f32 v79, v79, s14, v78
	v_cvt_pk_fp8_f32 v81, v82, v79 op_sel:[0,0,1]
	v_mul_f32_e32 v79, 0x42800000, v14
	v_mul_f32_e32 v82, 0x42800000, v46
	v_med3_f32 v79, v79, s14, v78
	v_med3_f32 v84, v82, s14, v78
	v_mov_b32_e32 v82, 0
	v_cvt_pk_fp8_f32 v82, v79, v84
	v_mul_f32_e32 v83, 0x42800000, v10
	v_mul_f32_e32 v79, 0x42800000, v42
	v_med3_f32 v83, v83, s14, v78
	v_med3_f32 v79, v79, s14, v78
	v_cvt_pk_fp8_f32 v82, v83, v79 op_sel:[0,0,1]
	v_mul_f32_e32 v79, 0x42800000, v6
	v_mul_f32_e32 v83, 0x42800000, v38
	v_med3_f32 v79, v79, s14, v78
	v_med3_f32 v85, v83, s14, v78
	v_mov_b32_e32 v83, 0
	v_cvt_pk_fp8_f32 v83, v79, v85
	v_mul_f32_e32 v84, 0x42800000, v2
	v_mul_f32_e32 v79, 0x42800000, v34
	s_bitcmp1_b32 s16, 0
	v_med3_f32 v84, v84, s14, v78
	v_med3_f32 v79, v79, s14, v78
	s_cselect_b32 s2, 0x9000, 0
	v_cvt_pk_fp8_f32 v83, v84, v79 op_sel:[0,0,1]
	s_add_i32 s17, s2, 0
	s_add_i32 s2, s12, s17
	v_add_u32_e32 v79, s2, v76
	ds_write_b128 v79, v[80:83]
	v_mul_f32_e32 v80, 0x42800000, v63
	v_mul_f32_e32 v81, 0x42800000, v31
	v_med3_f32 v83, v80, s14, v78
	v_med3_f32 v81, v81, s14, v78
	v_mov_b32_e32 v80, 0
	v_cvt_pk_fp8_f32 v80, v83, v81
	v_mul_f32_e32 v82, 0x42800000, v27
	v_mul_f32_e32 v81, 0x42800000, v59
	v_med3_f32 v82, v82, s14, v78
	v_med3_f32 v81, v81, s14, v78
	v_cvt_pk_fp8_f32 v80, v82, v81 op_sel:[0,0,1]
	v_mul_f32_e32 v81, 0x42800000, v23
	v_mul_f32_e32 v82, 0x42800000, v55
	v_med3_f32 v84, v81, s14, v78
	v_med3_f32 v82, v82, s14, v78
	v_mov_b32_e32 v81, 0
	v_cvt_pk_fp8_f32 v81, v84, v82
	v_mul_f32_e32 v83, 0x42800000, v19
	v_mul_f32_e32 v82, 0x42800000, v51
	v_med3_f32 v83, v83, s14, v78
	v_med3_f32 v82, v82, s14, v78
	v_cvt_pk_fp8_f32 v81, v83, v82 op_sel:[0,0,1]
	v_mul_f32_e32 v82, 0x42800000, v15
	v_mul_f32_e32 v83, 0x42800000, v47
	v_med3_f32 v85, v82, s14, v78
	v_med3_f32 v83, v83, s14, v78
	v_mov_b32_e32 v82, 0
	v_cvt_pk_fp8_f32 v82, v85, v83
	v_mul_f32_e32 v84, 0x42800000, v11
	v_mul_f32_e32 v83, 0x42800000, v43
	v_med3_f32 v84, v84, s14, v78
	v_med3_f32 v83, v83, s14, v78
	v_cvt_pk_fp8_f32 v82, v84, v83 op_sel:[0,0,1]
	v_mul_f32_e32 v83, 0x42800000, v7
	v_mul_f32_e32 v84, 0x42800000, v39
	v_med3_f32 v86, v83, s14, v78
	v_med3_f32 v84, v84, s14, v78
	v_mov_b32_e32 v83, 0
	v_cvt_pk_fp8_f32 v83, v86, v84
	v_mul_f32_e32 v85, 0x42800000, v3
	v_mul_f32_e32 v84, 0x42800000, v35
	v_med3_f32 v85, v85, s14, v78
	v_med3_f32 v84, v84, s14, v78
	v_cvt_pk_fp8_f32 v83, v85, v84 op_sel:[0,0,1]
	v_mul_f32_e32 v84, 0x42800000, v64
	v_mul_f32_e32 v85, 0x42800000, v32
	v_med3_f32 v87, v84, s14, v78
	v_med3_f32 v85, v85, s14, v78
	v_mov_b32_e32 v84, 0
	v_cvt_pk_fp8_f32 v84, v87, v85
	v_mul_f32_e32 v86, 0x42800000, v28
	v_mul_f32_e32 v85, 0x42800000, v60
	v_med3_f32 v86, v86, s14, v78
	v_med3_f32 v85, v85, s14, v78
	v_cvt_pk_fp8_f32 v84, v86, v85 op_sel:[0,0,1]
	v_mul_f32_e32 v85, 0x42800000, v24
	v_mul_f32_e32 v86, 0x42800000, v56
	v_med3_f32 v88, v85, s14, v78
	v_med3_f32 v86, v86, s14, v78
	v_mov_b32_e32 v85, 0
	v_cvt_pk_fp8_f32 v85, v88, v86
	v_mul_f32_e32 v87, 0x42800000, v20
	v_mul_f32_e32 v86, 0x42800000, v52
	v_med3_f32 v87, v87, s14, v78
	v_med3_f32 v86, v86, s14, v78
	v_cvt_pk_fp8_f32 v85, v87, v86 op_sel:[0,0,1]
	v_mul_f32_e32 v86, 0x42800000, v16
	v_mul_f32_e32 v87, 0x42800000, v48
	v_med3_f32 v89, v86, s14, v78
	v_med3_f32 v87, v87, s14, v78
	v_mov_b32_e32 v86, 0
	v_cvt_pk_fp8_f32 v86, v89, v87
	v_mul_f32_e32 v88, 0x42800000, v12
	v_mul_f32_e32 v87, 0x42800000, v44
	v_med3_f32 v88, v88, s14, v78
	v_med3_f32 v87, v87, s14, v78
	v_cvt_pk_fp8_f32 v86, v88, v87 op_sel:[0,0,1]
	v_mul_f32_e32 v87, 0x42800000, v8
	v_mul_f32_e32 v88, 0x42800000, v40
	v_med3_f32 v90, v87, s14, v78
	v_med3_f32 v88, v88, s14, v78
	v_mov_b32_e32 v87, 0
	v_cvt_pk_fp8_f32 v87, v90, v88
	v_mul_f32_e32 v89, 0x42800000, v4
	v_mul_f32_e32 v88, 0x42800000, v36
	v_med3_f32 v89, v89, s14, v78
	v_med3_f32 v88, v88, s14, v78
	v_cvt_pk_fp8_f32 v87, v89, v88 op_sel:[0,0,1]
	v_mul_f32_e32 v88, 0x42800000, v65
	v_mul_f32_e32 v89, 0x42800000, v33
	v_med3_f32 v91, v88, s14, v78
	v_med3_f32 v89, v89, s14, v78
	v_mov_b32_e32 v88, 0
	v_cvt_pk_fp8_f32 v88, v91, v89
	v_mul_f32_e32 v90, 0x42800000, v29
	v_mul_f32_e32 v89, 0x42800000, v61
	v_med3_f32 v90, v90, s14, v78
	v_med3_f32 v89, v89, s14, v78
	v_cvt_pk_fp8_f32 v88, v90, v89 op_sel:[0,0,1]
	v_mul_f32_e32 v89, 0x42800000, v25
	v_mul_f32_e32 v90, 0x42800000, v57
	v_med3_f32 v92, v89, s14, v78
	v_med3_f32 v90, v90, s14, v78
	v_mov_b32_e32 v89, 0
	v_cvt_pk_fp8_f32 v89, v92, v90
	v_mul_f32_e32 v91, 0x42800000, v21
	v_mul_f32_e32 v90, 0x42800000, v53
	v_med3_f32 v91, v91, s14, v78
	v_med3_f32 v90, v90, s14, v78
	v_cvt_pk_fp8_f32 v89, v91, v90 op_sel:[0,0,1]
	v_mul_f32_e32 v90, 0x42800000, v17
	v_mul_f32_e32 v91, 0x42800000, v49
	v_med3_f32 v93, v90, s14, v78
	v_med3_f32 v91, v91, s14, v78
	v_mov_b32_e32 v90, 0
	v_cvt_pk_fp8_f32 v90, v93, v91
	v_mul_f32_e32 v92, 0x42800000, v13
	v_mul_f32_e32 v91, 0x42800000, v45
	v_med3_f32 v92, v92, s14, v78
	v_med3_f32 v91, v91, s14, v78
	v_cvt_pk_fp8_f32 v90, v92, v91 op_sel:[0,0,1]
	v_mul_f32_e32 v91, 0x42800000, v9
	v_mul_f32_e32 v92, 0x42800000, v41
	v_med3_f32 v94, v91, s14, v78
	v_med3_f32 v92, v92, s14, v78
	v_mov_b32_e32 v91, 0
	v_cvt_pk_fp8_f32 v91, v94, v92
	v_mul_f32_e32 v93, 0x42800000, v5
	v_mul_f32_e32 v92, 0x42800000, v37
	v_med3_f32 v93, v93, s14, v78
	v_med3_f32 v92, v92, s14, v78
	v_cvt_pk_fp8_f32 v91, v93, v92 op_sel:[0,0,1]
	s_cmp_gt_u32 s16, 1
	ds_write_b128 v79, v[80:83] offset:144
	ds_write_b128 v79, v[84:87] offset:288
	ds_write_b128 v79, v[88:91] offset:432
	s_cbranch_scc1 .LBB0_476
; __device__ __forceinline__ Cvb conv8b_dec(const Ctx& X, int bit) { Cvb c; int kb, nb;
;     if (bit < I_GU8 / 8) { const int e = bit >> 8, r = bit & 255; kb = r >> 4; nb = r & 15; c.N = 2 * DFF; c.W = XP_w_gu(X) + (size_t)e * D * (2 * DFF); c.WT = XP_WguT(X) + (size_t)e * 16 * PAN_GU + (size_t)kb * PAN_GU; }
;     else { const int b2 = bit - I_GU8 / 8, e = b2 >> 7, r = b2 & 127; kb = r >> 3; nb = r & 7; c.N = D; c.W = XP_w_d(X) + (size_t)e * DFF * D; c.WT = XP_WdT(X) + (size_t)e * 16 * PAN_D + (size_t)kb * PAN_D; }
;     c.W += (size_t)(kb * 128 + 16 * X.wave) * c.N + nb * 256 + 4 * X.lane;
;     c.WT += (size_t)(nb * 256 + 32 * X.wave + (X.lane >> 3)) * 128 + 16 * (X.lane & 7);
; __device__ __forceinline__ void conv8b_run(const Ctx& X, int first, int step, int count) {
;     ...
;         if (j + 1 < count) { cn = conv8b_dec(X, first + (j + 1) * step);
; #pragma unroll
;             for (int i = 0; i < 16; ++i) v[i] = __builtin_nontemporal_load((const f32x4*)(cn.W + (size_t)i * cn.N)); }
	s_add_i32 s2, s13, 0xffffe000
	s_load_dwordx2 s[6:7], s[0:1], 0x80
	s_bfe_u32 s18, s13, 0x40003
	s_lshr_b32 s2, s2, 7
	s_lshl_b32 s19, s18, 18
	s_lshl_b64 s[8:9], s[2:3], 22
	s_add_u32 s20, s10, s8
	s_addc_u32 s21, s11, s9
	s_lshl_b64 s[8:9], s[2:3], 24
	s_waitcnt lgkmcnt(0)
	s_add_u32 s22, s6, s8
	s_addc_u32 s23, s7, s9
	s_add_u32 s6, s20, s19
	s_addc_u32 s7, s21, 0
	s_lshl_b32 s2, s18, 7
	s_add_i32 s2, s2, s12
	s_lshl_b64 s[8:9], s[2:3], 13
	s_add_u32 s2, s22, s8
	s_addc_u32 s9, s23, s9
	s_add_u32 s8, s2, s15
	s_addc_u32 s9, s9, 0
	v_lshl_add_u64 v[34:35], s[8:9], 0, v[66:67]
	v_add_co_u32_e32 v2, vcc, 0x2000, v34
	s_nop 1
	v_addc_co_u32_e32 v3, vcc, 0, v35, vcc
	v_add_co_u32_e32 v4, vcc, 0x4000, v34
	s_nop 1
	v_addc_co_u32_e32 v5, vcc, 0, v35, vcc
	global_load_dwordx4 v[30:33], v[2:3], off nt
	global_load_dwordx4 v[26:29], v[4:5], off nt
	v_add_co_u32_e32 v2, vcc, 0x6000, v34
	s_nop 1
	v_addc_co_u32_e32 v3, vcc, 0, v35, vcc
	v_add_co_u32_e32 v4, vcc, 0x8000, v34
	s_nop 1
	v_addc_co_u32_e32 v5, vcc, 0, v35, vcc
	global_load_dwordx4 v[58:61], v[2:3], off nt
	global_load_dwordx4 v[22:25], v[4:5], off nt
	v_add_co_u32_e32 v2, vcc, 0xa000, v34
	s_nop 1
	v_addc_co_u32_e32 v3, vcc, 0, v35, vcc
	v_add_co_u32_e32 v4, vcc, 0xc000, v34
	s_nop 1
	v_addc_co_u32_e32 v5, vcc, 0, v35, vcc
	global_load_dwordx4 v[54:57], v[2:3], off nt
	global_load_dwordx4 v[18:21], v[4:5], off nt
	v_add_co_u32_e32 v2, vcc, 0xe000, v34
	s_nop 1
	v_addc_co_u32_e32 v3, vcc, 0, v35, vcc
	v_add_co_u32_e32 v4, vcc, 0x10000, v34
	s_nop 1
	v_addc_co_u32_e32 v5, vcc, 0, v35, vcc
	global_load_dwordx4 v[50:53], v[2:3], off nt
	global_load_dwordx4 v[14:17], v[4:5], off nt
	v_add_co_u32_e32 v2, vcc, 0x12000, v34
	s_nop 1
	v_addc_co_u32_e32 v3, vcc, 0, v35, vcc
	v_add_co_u32_e32 v4, vcc, 0x14000, v34
	s_nop 1
	v_addc_co_u32_e32 v5, vcc, 0, v35, vcc
	global_load_dwordx4 v[46:49], v[2:3], off nt
	global_load_dwordx4 v[10:13], v[4:5], off nt
	v_add_co_u32_e32 v2, vcc, 0x16000, v34
	s_nop 1
	v_addc_co_u32_e32 v3, vcc, 0, v35, vcc
	v_add_co_u32_e32 v4, vcc, 0x18000, v34
	s_nop 1
	v_addc_co_u32_e32 v5, vcc, 0, v35, vcc
	v_add_co_u32_e32 v36, vcc, 0x1a000, v34
	global_load_dwordx4 v[42:45], v[2:3], off nt
	global_load_dwordx4 v[6:9], v[4:5], off nt
	v_addc_co_u32_e32 v37, vcc, 0, v35, vcc
	v_add_co_u32_e32 v62, vcc, 0x1c000, v34
	s_nop 1
	v_addc_co_u32_e32 v63, vcc, 0, v35, vcc
	v_add_co_u32_e32 v74, vcc, 0x1e000, v34
	global_load_dwordx4 v[38:41], v[36:37], off nt
	global_load_dwordx4 v[2:5], v[62:63], off nt
	v_addc_co_u32_e32 v75, vcc, 0, v35, vcc
	global_load_dwordx4 v[62:65], v66, s[8:9] nt
	global_load_dwordx4 v[34:37], v[74:75], off nt
	v_lshl_add_u64 v[74:75], s[6:7], 0, v[70:71]
	v_lshl_add_u64 v[74:75], v[74:75], 0, v[68:69]
	s_branch .LBB0_476
